# static priority raise for the staging waves (4-7) during light-tile K-loops
# baseline (speedup 1.0000x reference)
; __device__ __forceinline__ __amdgpu_buffer_rsrc_t mk_rsrc(const void* p) { return __builtin_amdgcn_make_buffer_rsrc((void*)p, 0, 0x7ffffff0, 0x00020000); }
; __device__ __forceinline__ int vwg_id() { const int G = gridDim.x; return (G % 8 == 0) ? (int)((blockIdx.x % 8) * (G / 8) + blockIdx.x / 8) : (int)blockIdx.x; }
; __device__ __forceinline__ void phase_moe_gu(const Ptrs& p, LAS unsigned char* lds) {
;     ...
;     for (int u = vwg_id(); moe_unit(cv, u, 16, mu); u += gridDim.x) {
;         GemmT T; T.init();
;         const int* list = (const int*)(p.ws + OFF_LIST) + (size_t)mu.e * NTOK; const int i0 = mu.mt * 256, n0 = mu.nt * 128;
;         unsigned ao[4];
; #pragma unroll
;         for (int i = 0; i < 4; ++i) { const int r = i0 + T.aR + 64 * i; const int tok = (r < mu.cnt) ? (list[r] >> 2) : 0; ao[i] = (unsigned)((tok * D + T.aC) * 2); }
;         const float* wsel = ((__builtin_amdgcn_readfirstlane(T.b_p) & 1) ? p.w_up : p.w_gate) + (size_t)mu.e * D * D + n0;
;         const unsigned bo = (unsigned)((T.b_k * D + T.b_gucol) * 4);
;         f32x4 acc[8][4]; acc_zero(acc);
;         const int mlim = __builtin_amdgcn_readfirstlane(T.wr) ? 0 : ((mu.cnt - i0 + 15) >> 4);
;         if (mu.light) gemm_kloop_light(acc, lds, T, mk_rsrc(h2), ao[0], ao[1], ao[2], ao[3], mk_rsrc(wsel), bo, D * 4u, D / 64, mlim);
.LBB0_1163:
	s_andn2_b64 vcc, exec, s[0:1]
	s_mov_b64 s[0:1], -1
	s_cbranch_vccnz .LBB0_1005
	s_ashr_i32 s43, s42, 31
	s_lshl_b64 s[0:1], s[42:43], 15
	v_mov_b32_e32 v3, v0
	s_add_u32 s0, s52, s0
	s_addc_u32 s1, s53, s1
	v_bfe_u32 v4, v3, 2, 4
	s_lshl_b32 s2, s86, 8
	v_ashrrev_i32_e32 v10, 7, v3
	v_or_b32_e32 v4, s2, v4
	v_lshl_add_u32 v4, v10, 4, v4
	v_cmp_gt_i32_e32 vcc, s87, v4
	v_mov_b32_e32 v6, 0
	v_ashrrev_i32_e32 v5, 31, v4
	v_mov_b32_e32 v7, 0
	v_mov_b32_e32 v8, 0
	v_mov_b32_e32 v9, 0
	v_lshl_add_u64 v[12:13], v[4:5], 2, s[0:1]
	s_and_saveexec_b64 s[4:5], vcc
	global_load_dword v7, v[12:13], off
	s_or_b64 exec, exec, s[4:5]
	v_add_u32_e32 v11, 64, v4
	v_cmp_gt_i32_e32 vcc, s87, v11
	s_and_saveexec_b64 s[4:5], vcc
	global_load_dword v6, v[12:13], off offset:256
	s_or_b64 exec, exec, s[4:5]
	v_add_u32_e32 v11, 0x80, v4
	v_cmp_gt_i32_e32 vcc, s87, v11
	s_and_saveexec_b64 s[4:5], vcc
	global_load_dword v9, v[12:13], off offset:512
	s_or_b64 exec, exec, s[4:5]
	v_add_u32_e32 v11, 0xc0, v4
	v_cmp_gt_i32_e32 vcc, s87, v11
	s_and_saveexec_b64 s[4:5], vcc
	global_load_dword v8, v[12:13], off offset:768
	s_or_b64 exec, exec, s[4:5]
	v_ashrrev_i32_e32 v5, 6, v3
	v_and_b32_e32 v11, 1, v5
	s_lshl_b32 s0, s85, 7
	v_readfirstlane_b32 s1, v11
	v_readlane_b32 s4, v246, 0
	s_bitcmp0_b32 s1, 0
	v_readlane_b32 s5, v246, 1
	s_cselect_b32 s1, s49, s5
	s_cselect_b32 s3, s48, s4
	s_lshl_b64 s[4:5], s[42:43], 24
	v_readlane_b32 s6, v246, 2
	s_add_u32 s3, s3, s4
	v_and_b32_e32 v4, 63, v3
	s_addc_u32 s6, s1, s5
	s_ashr_i32 s1, s0, 31
	v_lshrrev_b32_e32 v12, 5, v4
	v_bfe_u32 v13, v3, 1, 2
	s_lshl_b64 s[4:5], s[0:1], 2
	v_lshl_or_b32 v10, v10, 1, v12
	v_bfe_u32 v12, v3, 3, 2
	v_and_b32_e32 v14, 1, v3
	v_lshlrev_b32_e32 v15, 5, v13
	s_add_u32 s24, s3, s4
	v_lshl_or_b32 v15, v12, 7, v15
	v_lshlrev_b32_e32 v16, 16, v10
	v_lshlrev_b32_e32 v17, 4, v14
	s_addc_u32 s1, s6, s5
	v_or3_b32 v225, v15, v17, v16
	s_and_b32 s25, s1, 0xffff
	s_movk_i32 s1, 0x2000
	buffer_load_dwordx4 v[114:117], v225, s[24:27], 0 offen
	buffer_load_dwordx4 v[118:121], v225, s[24:27], s66 offen
	s_mov_b32 s3, 0x8000
	buffer_load_dwordx4 v[126:129], v225, s[24:27], s1 offen
	buffer_load_dwordx4 v[122:125], v225, s[24:27], s3 offen
	s_movk_i32 s1, 0x4000
	s_mov_b32 s3, 0xa000
	buffer_load_dwordx4 v[130:133], v225, s[24:27], s1 offen
	buffer_load_dwordx4 v[134:137], v225, s[24:27], s3 offen
	s_mov_b32 s1, 0xc000
	s_mov_b32 s3, 0xe000
	buffer_load_dwordx4 v[142:145], v225, s[24:27], s1 offen
	buffer_load_dwordx4 v[146:149], v225, s[24:27], s3 offen
	s_waitcnt vmcnt(8)
	v_lshlrev_b32_e32 v7, 10, v7
	v_and_b32_e32 v7, 0xfffff000, v7
	v_lshlrev_b32_e32 v6, 10, v6
	v_and_b32_e32 v6, 0xfffff000, v6
	v_lshlrev_b32_e32 v9, 10, v9
	v_and_b32_e32 v9, 0xfffff000, v9
	v_lshlrev_b32_e32 v8, 10, v8
	v_and_b32_e32 v8, 0xfffff000, v8
	v_lshlrev_b32_e32 v17, 4, v3
	v_lshlrev_b32_e32 v15, 6, v11
	v_and_b32_e32 v16, 32, v3
	v_and_b32_e32 v17, 48, v17
	v_bitop3_b32 v15, v17, v15, v16 bitop3:0xde
	v_or_b32_e32 v221, v9, v15
	v_lshlrev_b32_e32 v9, 2, v12
	v_lshlrev_b32_e32 v11, 1, v11
	v_or3_b32 v9, v9, v11, v14
	v_lshlrev_b32_e32 v11, 2, v3
	v_and_b32_e32 v12, 0xfffffc00, v11
	v_lshl_add_u32 v9, v9, 11, v12
	v_lshlrev_b32_e32 v12, 8, v13
	v_lshlrev_b32_e32 v10, 4, v10
	v_and_or_b32 v10, v10, 48, v12
	v_lshlrev_b32_e32 v12, 3, v3
	v_or_b32_e32 v223, v7, v15
	v_and_b32_e32 v7, 15, v3
	v_and_b32_e32 v12, 32, v12
	v_or_b32_e32 v222, v6, v15
	v_ashrrev_i32_e32 v6, 8, v3
	v_bitop3_b32 v219, v9, v10, v12 bitop3:0xf6
	v_lshlrev_b32_e32 v7, 6, v7
	v_and_b32_e32 v3, 48, v3
	v_and_b32_e32 v10, 32, v11
	v_or_b32_e32 v9, v7, v3
	v_bitop3_b32 v3, v7, v10, v3 bitop3:0x36
	v_lshlrev_b32_e32 v11, 13, v5
	v_lshlrev_b32_e32 v220, 6, v14
	v_lshlrev_b32_e32 v4, 4, v4
	v_lshlrev_b32_e32 v7, 14, v6
	v_and_or_b32 v226, v11, s66, v3
	v_cmp_eq_u32_e32 vcc, 0, v215
	v_add_u32_e32 v227, 0, v219
	v_add_u32_e32 v3, 0xc0, v220
	v_or_b32_e32 v224, v8, v15
	v_lshl_or_b32 v229, v5, 10, v4
	v_bitop3_b32 v216, v9, v7, v10 bitop3:0xde
	v_or_b32_e32 v217, 0x8000, v226
	v_readfirstlane_b32 s1, v6
	s_and_b64 vcc, exec, vcc
	v_add_u32_e32 v228, v227, v220
	v_and_b32_e32 v218, 0xc0, v3
	v_readlane_b32 s7, v246, 3
	v_readlane_b32 s8, v246, 4
	v_readlane_b32 s9, v246, 5
	v_readlane_b32 s10, v246, 6
	v_readlane_b32 s11, v246, 7
	s_cbranch_vccnz .LBB0_1263
	s_sub_i32 s3, s87, s2
	s_mov_b32 s99, s3
	v_readfirstlane_b32 s100, v0
	s_nop 3
	s_lshr_b32 s100, s100, 7
	s_lshl_b32 s100, s100, 4
	s_add_i32 s3, s3, 15
	s_cmp_ge_i32 s100, 32
	s_cbranch_scc0 .Lmy_sp0
	s_setprio 1

; __device__ __forceinline__ int tid_opaque() { int t = threadIdx.x; asm volatile("" : "+v"(t)); return t; }
; __device__ __forceinline__ __amdgpu_buffer_rsrc_t mk_rsrc(const void* p) { return __builtin_amdgcn_make_buffer_rsrc((void*)p, 0, 0x7ffffff0, 0x00020000); }
; __device__ __forceinline__ void phase_moe_down(const Ptrs& p, LAS unsigned char* lds) {
;     ...
;         GemmT T; T.init();
;         const int* list = (const int*)(p.ws + OFF_LIST) + (size_t)mu.e * NTOK; const int i0 = mu.mt * 256, col0 = mu.nt * 256;
;         const unsigned ao = (unsigned)((T.aR * D + T.aC) * 2), bo = (unsigned)((T.b_k * D + T.b_col) * 4);
;         int pa = -1; float pg = 0.f;
;         { const int t_ = tid_opaque(); if (t_ < 256 && i0 + t_ < mu.cnt) { pa = list[i0 + t_]; pg = gate[pa]; } }
;         f32x4 acc[8][4]; acc_zero(acc);
;         const int mlim = __builtin_amdgcn_readfirstlane(T.wr) ? 0 : ((mu.cnt - i0 + 15) >> 4);
;         if (mu.light) gemm_kloop_light(acc, lds, T, mk_rsrc(act + (size_t)(mu.base + i0) * D), ao, ao + 64u * 4096, ao + 128u * 4096, ao + 192u * 4096,
;                                        mk_rsrc(p.w_down + (size_t)mu.e * D * D + col0), bo, D * 4u, D / 64, mlim);
.LBB0_1483:
	s_or_b64 exec, exec, s[0:1]
	s_add_i32 s2, s84, s85
	s_ashr_i32 s3, s2, 31
	s_lshl_b32 s0, s81, 8
	s_lshl_b64 s[2:3], s[2:3], 12
	s_add_u32 s36, s20, s2
	v_readlane_b32 s4, v246, 0
	s_addc_u32 s1, s28, s3
	v_readlane_b32 s5, v246, 1
	v_readlane_b32 s6, v246, 2
	v_readlane_b32 s7, v246, 3
	v_readlane_b32 s8, v246, 4
	v_readlane_b32 s9, v246, 5
	s_and_b32 s37, s1, 0xffff
	s_lshl_b64 s[2:3], s[42:43], 24
	v_readlane_b32 s10, v246, 6
	v_readlane_b32 s11, v246, 7
	s_mov_b64 s[4:5], s[8:9]
	s_add_u32 s4, s4, s2
	v_ashrrev_i32_e32 v4, 6, v3
	v_bfe_u32 v11, v3, 1, 2
	s_addc_u32 s5, s5, s3
	s_ashr_i32 s1, s0, 31
	v_ashrrev_i32_e32 v5, 7, v3
	v_and_b32_e32 v6, 1, v4
	v_bfe_u32 v8, v3, 5, 1
	v_bfe_u32 v10, v3, 3, 2
	v_and_b32_e32 v12, 1, v3
	v_lshlrev_b32_e32 v14, 3, v11
	s_lshl_b64 s[2:3], s[0:1], 2
	v_lshlrev_b32_e32 v7, 5, v6
	v_lshl_or_b32 v9, v5, 1, v8
	v_lshl_or_b32 v14, v10, 6, v14
	v_lshlrev_b32_e32 v15, 2, v12
	s_add_u32 s24, s4, s2
	v_lshlrev_b32_e32 v13, 16, v9
	v_or3_b32 v14, v14, v15, v7
	s_addc_u32 s1, s5, s3
	v_lshl_or_b32 v222, v14, 2, v13
	s_and_b32 s25, s1, 0xffff
	s_movk_i32 s1, 0x2000
	buffer_load_dwordx4 v[110:113], v222, s[24:27], 0 offen
	buffer_load_dwordx4 v[114:117], v222, s[24:27], s66 offen
	s_mov_b32 s2, 0x8000
	buffer_load_dwordx4 v[122:125], v222, s[24:27], s1 offen
	buffer_load_dwordx4 v[118:121], v222, s[24:27], s2 offen
	s_movk_i32 s1, 0x4000
	s_mov_b32 s2, 0xa000
	buffer_load_dwordx4 v[126:129], v222, s[24:27], s1 offen
	buffer_load_dwordx4 v[130:133], v222, s[24:27], s2 offen
	s_mov_b32 s1, 0xc000
	s_mov_b32 s2, 0xe000
	buffer_load_dwordx4 v[138:141], v222, s[24:27], s1 offen
	buffer_load_dwordx4 v[142:145], v222, s[24:27], s2 offen
	s_waitcnt vmcnt(8)
	v_cmp_ne_u32_e32 vcc, -1, v214
	s_and_saveexec_b64 vcc, vcc
	v_ashrrev_i32_e32 v17, 31, v214
	v_mov_b32_e32 v16, v214
	v_lshl_add_u64 v[16:17], v[16:17], 2, s[56:57]
	global_load_dword v215, v[16:17], off
	s_or_b64 exec, exec, vcc
	v_lshlrev_b32_e32 v16, 3, v3
	v_and_b32_e32 v13, 63, v3
	v_lshlrev_b32_e32 v8, 4, v8
	v_and_b32_e32 v17, 24, v16
	v_bitop3_b32 v7, v8, v7, v17 bitop3:0xde
	v_lshlrev_b32_e32 v8, 4, v13
	v_lshl_or_b32 v230, v4, 10, v8
	v_lshlrev_b32_e32 v8, 2, v10
	v_lshlrev_b32_e32 v6, 1, v6
	v_or3_b32 v6, v8, v6, v12
	v_lshlrev_b32_e32 v8, 2, v3
	v_and_b32_e32 v10, 0xfffffc00, v8
	v_lshl_add_u32 v6, v6, 11, v10
	v_lshlrev_b32_e32 v10, 8, v11
	v_lshlrev_b32_e32 v9, 4, v9
	v_and_b32_e32 v15, 15, v3
	v_and_or_b32 v9, v9, 48, v10
	v_and_b32_e32 v10, 32, v16
	v_bitop3_b32 v220, v6, v9, v10 bitop3:0xf6
	v_lshlrev_b32_e32 v6, 6, v15
	v_and_b32_e32 v9, 48, v3
	v_and_b32_e32 v8, 32, v8
	v_or_b32_e32 v10, v6, v9
	v_bitop3_b32 v6, v6, v8, v9 bitop3:0x36
	v_lshlrev_b32_e32 v4, 13, v4
	v_ashrrev_i32_e32 v14, 8, v3
	v_and_or_b32 v227, v4, s66, v6
	v_lshlrev_b32_e32 v4, 16, v5
	v_lshlrev_b32_e32 v3, 10, v3
	s_mov_b32 s1, 0xf000
	v_lshlrev_b32_e32 v219, 6, v12
	v_and_or_b32 v3, v3, s1, v4
	v_lshlrev_b32_e32 v9, 14, v14
	v_lshl_or_b32 v225, v7, 1, v3
	v_cmp_eq_u32_e32 vcc, 0, v216
	v_add_u32_e32 v228, 0, v220
	v_add_u32_e32 v3, 0xc0, v219
	v_bitop3_b32 v217, v10, v9, v8 bitop3:0xde
	v_or_b32_e32 v218, 0x8000, v227
	v_readfirstlane_b32 s1, v14
	v_add_u32_e32 v226, 0x40000, v225
	v_add_u32_e32 v224, 0x80000, v225
	v_add_u32_e32 v223, 0xc0000, v225
	v_add_u32_e32 v229, v228, v219
	v_and_b32_e32 v221, 0xc0, v3
	s_mov_b64 s[6:7], s[10:11]
	s_cbranch_vccnz .LBB0_1574
	s_sub_i32 s2, s83, s85
	s_mov_b32 s99, s2
	v_readfirstlane_b32 s100, v0
	s_nop 3
	s_lshr_b32 s100, s100, 7
	s_lshl_b32 s100, s100, 4
	s_add_i32 s2, s2, 15
	s_cmp_ge_i32 s100, 32
	s_cbranch_scc0 .Lmy_sp1
	s_setprio 1
